# xq-GEMM epilogue: 32 row-statistic loads issued together with counted waits; MoE gate-up: per-unit bias vectors prefetched before the K-loop, epilogue vmcnt(0) drain removed
# speedup vs baseline: 1.0192x; 1.0057x over previous
.LBB0_1673:
	v_lshl_add_u32 v84, s18, 7, v1
	v_readlane_b32 s48, v236, 24
	v_ashrrev_i32_e32 v85, 31, v84
	v_readlane_b32 s50, v236, 26
	v_readlane_b32 s51, v236, 27
	s_lshl_b32 s18, s19, 8
	s_ashr_i32 s19, s18, 31
	v_lshl_add_u64 v[100:101], v[84:85], 4, s[50:51]
	global_load_dwordx4 v[106:109], v[100:101], off
	global_load_dwordx4 v[138:141], v[100:101], off offset:256
	global_load_dwordx4 v[170:173], v[100:101], off offset:512
	global_load_dwordx4 v[202:205], v[100:101], off offset:768
	v_add_co_u32_e32 v234, vcc, s39, v100
	s_nop 1
	v_addc_co_u32_e32 v235, vcc, 0, v101, vcc
	global_load_dwordx4 v[110:113], v[234:235], off
	global_load_dwordx4 v[142:145], v[234:235], off offset:256
	global_load_dwordx4 v[174:177], v[234:235], off offset:512
	global_load_dwordx4 v[206:209], v[234:235], off offset:768
	v_add_co_u32_e32 v234, vcc, s40, v100
	s_nop 1
	v_addc_co_u32_e32 v235, vcc, 0, v101, vcc
	global_load_dwordx4 v[114:117], v[234:235], off
	global_load_dwordx4 v[146:149], v[234:235], off offset:256
	global_load_dwordx4 v[178:181], v[234:235], off offset:512
	global_load_dwordx4 v[210:213], v[234:235], off offset:768
	v_add_co_u32_e32 v234, vcc, s41, v100
	s_nop 1
	v_addc_co_u32_e32 v235, vcc, 0, v101, vcc
	global_load_dwordx4 v[118:121], v[234:235], off
	global_load_dwordx4 v[150:153], v[234:235], off offset:256
	global_load_dwordx4 v[182:185], v[234:235], off offset:512
	global_load_dwordx4 v[214:217], v[234:235], off offset:768
	v_add_co_u32_e32 v234, vcc, s42, v100
	s_nop 1
	v_addc_co_u32_e32 v235, vcc, 0, v101, vcc
	global_load_dwordx4 v[122:125], v[234:235], off
	global_load_dwordx4 v[154:157], v[234:235], off offset:256
	global_load_dwordx4 v[186:189], v[234:235], off offset:512
	global_load_dwordx4 v[218:221], v[234:235], off offset:768
	v_add_co_u32_e32 v234, vcc, s43, v100
	s_nop 1
	v_addc_co_u32_e32 v235, vcc, 0, v101, vcc
	global_load_dwordx4 v[126:129], v[234:235], off
	global_load_dwordx4 v[158:161], v[234:235], off offset:256
	global_load_dwordx4 v[190:193], v[234:235], off offset:512
	global_load_dwordx4 v[222:225], v[234:235], off offset:768
	v_add_co_u32_e32 v234, vcc, s44, v100
	s_nop 1
	v_addc_co_u32_e32 v235, vcc, 0, v101, vcc
	global_load_dwordx4 v[130:133], v[234:235], off
	global_load_dwordx4 v[162:165], v[234:235], off offset:256
	global_load_dwordx4 v[194:197], v[234:235], off offset:512
	global_load_dwordx4 v[226:229], v[234:235], off offset:768
	v_add_co_u32_e32 v234, vcc, s45, v100
	s_nop 1
	v_addc_co_u32_e32 v235, vcc, 0, v101, vcc
	global_load_dwordx4 v[134:137], v[234:235], off
	global_load_dwordx4 v[166:169], v[234:235], off offset:256
	global_load_dwordx4 v[198:201], v[234:235], off offset:512
	global_load_dwordx4 v[230:233], v[234:235], off offset:768
	s_nop 0
	v_readlane_b32 s54, v236, 30
	v_readlane_b32 s55, v236, 31
	s_lshl_b64 s[18:19], s[18:19], 1
	v_readlane_b32 s49, v236, 25
	v_readlane_b32 s52, v236, 28
	v_readlane_b32 s53, v236, 29
	s_waitcnt vmcnt(3)
	v_mov_b32_e32 v102, v106
	v_mov_b32_e32 v103, v110
	v_mov_b32_e32 v96, v107
	v_mov_b32_e32 v97, v111
	v_pk_add_f32 v[92:93], v[102:103], v[96:97]
	v_mov_b32_e32 v96, v108
	v_mov_b32_e32 v97, v112
	v_mov_b32_e32 v98, v109
	v_mov_b32_e32 v99, v113
	v_pk_add_f32 v[94:95], v[96:97], v[98:99]
	s_nop 0
	v_pk_add_f32 v[92:93], v[92:93], v[94:95]
	s_nop 0
	v_add_f32_e32 v86, 0, v92
	v_add_f32_e32 v96, v86, v93
	s_nop 0
	v_mov_b32_e32 v98, v115
	v_mov_b32_e32 v99, v116
	v_mov_b32_e32 v93, v117
	v_mov_b32_e32 v92, v114
	v_pk_add_f32 v[92:93], v[98:99], v[92:93]
	s_nop 0
	v_pk_add_f32 v[98:99], v[92:93], v[92:93] op_sel:[0,1] op_sel_hi:[1,0]
	s_nop 1
	v_add_f32_e32 v102, v118, v119
	v_add_f32_e32 v104, v120, v121
	s_nop 0
	v_mov_b32_e32 v97, v122
	v_mov_b32_e32 v99, v123
	v_mov_b32_e32 v103, v124
	v_mov_b32_e32 v105, v125
	v_pk_add_f32 v[92:93], v[96:97], v[98:99]
	v_pk_add_f32 v[94:95], v[102:103], v[104:105]
	s_nop 0
	v_pk_add_f32 v[92:93], v[92:93], v[94:95]
	s_nop 0
	v_pk_add_f32 v[96:97], v[92:93], v[92:93] op_sel:[0,1] op_sel_hi:[1,0]
	s_nop 1
	v_mov_b32_e32 v98, v127
	v_mov_b32_e32 v99, v128
	v_mov_b32_e32 v93, v129
	v_mov_b32_e32 v92, v126
	v_pk_add_f32 v[92:93], v[98:99], v[92:93]
	s_nop 0
	v_pk_add_f32 v[98:99], v[92:93], v[92:93] op_sel:[0,1] op_sel_hi:[1,0]
	s_nop 1
	v_add_f32_e32 v102, v130, v131
	v_add_f32_e32 v104, v132, v133
	s_nop 0
	v_mov_b32_e32 v97, v134
	v_mov_b32_e32 v99, v135
	v_mov_b32_e32 v103, v136
	v_mov_b32_e32 v105, v137
	v_pk_add_f32 v[92:93], v[96:97], v[98:99]
	v_pk_add_f32 v[94:95], v[102:103], v[104:105]
	s_nop 0
	v_pk_add_f32 v[92:93], v[92:93], v[94:95]
	s_nop 0
	v_add_f32_e32 v86, v92, v93
	v_fmamk_f32 v86, v86, 0x3a000000, v91
	v_rsq_f32_e32 v86, v86
	v_lshlrev_b64 v[92:93], 10, v[84:85]
	v_pk_mul_f32 v[62:63], v[62:63], v[86:87] op_sel_hi:[1,0]
	v_pk_mul_f32 v[94:95], v[60:61], v[86:87] op_sel_hi:[1,0]
	v_pk_mul_f32 v[60:61], v[58:59], v[86:87] op_sel_hi:[1,0]
	v_cvt_pk_bf16_f32 v58, v62, v63
	v_lshl_add_u64 v[62:63], s[54:55], 0, v[92:93]
	v_lshl_add_u64 v[62:63], v[62:63], 0, s[18:19]
	v_pk_mul_f32 v[64:65], v[64:65], v[86:87] op_sel_hi:[1,0]
	v_lshl_add_u64 v[62:63], v[62:63], 0, v[74:75]
	v_cvt_pk_bf16_f32 v59, v64, v65
	v_cvt_pk_bf16_f32 v60, v60, v61
	v_cvt_pk_bf16_f32 v61, v94, v95
	global_store_dwordx4 v[62:63], v[58:61], off
	v_pk_mul_f32 v[56:57], v[56:57], v[86:87] op_sel_hi:[1,0]
	v_pk_mul_f32 v[54:55], v[54:55], v[86:87] op_sel_hi:[1,0]
	v_pk_mul_f32 v[58:59], v[52:53], v[86:87] op_sel_hi:[1,0]
	v_pk_mul_f32 v[52:53], v[50:51], v[86:87] op_sel_hi:[1,0]
	v_cvt_pk_bf16_f32 v50, v54, v55
	v_cvt_pk_bf16_f32 v51, v56, v57
	s_nop 0
	v_cvt_pk_bf16_f32 v52, v52, v53
	v_cvt_pk_bf16_f32 v53, v58, v59
	v_or_b32_e32 v58, 16, v84
	v_ashrrev_i32_e32 v59, 31, v58
	v_lshl_add_u64 v[60:61], v[58:59], 4, s[50:51]
	global_store_dwordx4 v[62:63], v[50:53], off offset:256
	s_nop 0
	s_nop 0
	s_waitcnt vmcnt(4)
	v_mov_b32_e32 v62, v138
	v_mov_b32_e32 v63, v142
	v_mov_b32_e32 v54, v139
	v_mov_b32_e32 v55, v143
	v_pk_add_f32 v[50:51], v[62:63], v[54:55]
	v_mov_b32_e32 v54, v140
	v_mov_b32_e32 v55, v144
	v_mov_b32_e32 v56, v141
	v_mov_b32_e32 v57, v145
	v_pk_add_f32 v[52:53], v[54:55], v[56:57]
	s_nop 0
	v_pk_add_f32 v[50:51], v[50:51], v[52:53]
	s_nop 0
	v_add_f32_e32 v50, 0, v50
	v_add_f32_e32 v54, v50, v51
	s_nop 1
	v_mov_b32_e32 v56, v147
	v_mov_b32_e32 v57, v148
	v_mov_b32_e32 v51, v149
	v_mov_b32_e32 v50, v146
	v_pk_add_f32 v[50:51], v[56:57], v[50:51]
	s_nop 0
	v_pk_add_f32 v[56:57], v[50:51], v[50:51] op_sel:[0,1] op_sel_hi:[1,0]
	s_nop 1
	v_add_f32_e32 v62, v150, v151
	v_add_f32_e32 v64, v152, v153
	s_nop 0
	v_mov_b32_e32 v55, v154
	v_mov_b32_e32 v57, v155
	v_mov_b32_e32 v63, v156
	v_mov_b32_e32 v65, v157
	v_pk_add_f32 v[50:51], v[54:55], v[56:57]
	v_pk_add_f32 v[52:53], v[62:63], v[64:65]
	s_nop 0
	v_pk_add_f32 v[50:51], v[50:51], v[52:53]
	s_nop 0
	v_pk_add_f32 v[54:55], v[50:51], v[50:51] op_sel:[0,1] op_sel_hi:[1,0]
	s_nop 1
	v_mov_b32_e32 v56, v159
	v_mov_b32_e32 v57, v160
	v_mov_b32_e32 v51, v161
	v_mov_b32_e32 v50, v158
	v_pk_add_f32 v[50:51], v[56:57], v[50:51]
	s_nop 0
	v_pk_add_f32 v[56:57], v[50:51], v[50:51] op_sel:[0,1] op_sel_hi:[1,0]
	s_nop 1
	v_add_f32_e32 v62, v162, v163
	v_add_f32_e32 v64, v164, v165
	s_nop 0
	v_mov_b32_e32 v55, v166
	v_mov_b32_e32 v57, v167
	v_mov_b32_e32 v63, v168
	v_mov_b32_e32 v65, v169
	v_pk_add_f32 v[50:51], v[54:55], v[56:57]
	v_pk_add_f32 v[52:53], v[62:63], v[64:65]
	s_nop 0
	v_pk_add_f32 v[50:51], v[50:51], v[52:53]
	v_lshlrev_b64 v[52:53], 10, v[58:59]
	v_add_f32_e32 v50, v50, v51
	v_fmamk_f32 v50, v50, 0x3a000000, v91
	v_rsq_f32_e32 v50, v50
	s_nop 0
	v_pk_mul_f32 v[46:47], v[46:47], v[50:51] op_sel_hi:[1,0]
	v_pk_mul_f32 v[54:55], v[44:45], v[50:51] op_sel_hi:[1,0]
	v_pk_mul_f32 v[44:45], v[42:43], v[50:51] op_sel_hi:[1,0]
	v_cvt_pk_bf16_f32 v42, v46, v47
	v_lshl_add_u64 v[46:47], s[54:55], 0, v[52:53]
	v_lshl_add_u64 v[46:47], v[46:47], 0, s[18:19]
	v_pk_mul_f32 v[48:49], v[48:49], v[50:51] op_sel_hi:[1,0]
	v_lshl_add_u64 v[46:47], v[46:47], 0, v[74:75]
	v_cvt_pk_bf16_f32 v43, v48, v49
	v_cvt_pk_bf16_f32 v44, v44, v45
	v_cvt_pk_bf16_f32 v45, v54, v55
	global_store_dwordx4 v[46:47], v[42:45], off
	v_pk_mul_f32 v[40:41], v[40:41], v[50:51] op_sel_hi:[1,0]
	v_pk_mul_f32 v[38:39], v[38:39], v[50:51] op_sel_hi:[1,0]
	v_pk_mul_f32 v[42:43], v[36:37], v[50:51] op_sel_hi:[1,0]
	v_pk_mul_f32 v[36:37], v[34:35], v[50:51] op_sel_hi:[1,0]
	v_cvt_pk_bf16_f32 v34, v38, v39
	v_cvt_pk_bf16_f32 v35, v40, v41
	s_nop 0
	v_cvt_pk_bf16_f32 v36, v36, v37
	v_cvt_pk_bf16_f32 v37, v42, v43
	v_or_b32_e32 v42, 32, v84
	v_ashrrev_i32_e32 v43, 31, v42
	v_lshl_add_u64 v[44:45], v[42:43], 4, s[50:51]
	global_store_dwordx4 v[46:47], v[34:37], off offset:256
	s_nop 0
	s_nop 0
	s_waitcnt vmcnt(5)
	v_mov_b32_e32 v46, v170
	v_mov_b32_e32 v47, v174
	v_mov_b32_e32 v38, v171
	v_mov_b32_e32 v39, v175
	v_pk_add_f32 v[34:35], v[46:47], v[38:39]
	v_mov_b32_e32 v38, v172
	v_mov_b32_e32 v39, v176
	v_mov_b32_e32 v40, v173
	v_mov_b32_e32 v41, v177
	v_pk_add_f32 v[36:37], v[38:39], v[40:41]
	s_nop 0
	v_pk_add_f32 v[34:35], v[34:35], v[36:37]
	s_nop 0
	v_add_f32_e32 v34, 0, v34
	v_add_f32_e32 v38, v34, v35
	s_nop 1
	v_mov_b32_e32 v40, v179
	v_mov_b32_e32 v41, v180
	v_mov_b32_e32 v35, v181
	v_mov_b32_e32 v34, v178
	v_pk_add_f32 v[34:35], v[40:41], v[34:35]
	s_nop 0
	v_pk_add_f32 v[40:41], v[34:35], v[34:35] op_sel:[0,1] op_sel_hi:[1,0]
	s_nop 1
	v_add_f32_e32 v46, v182, v183
	v_add_f32_e32 v48, v184, v185
	s_nop 0
	v_mov_b32_e32 v39, v186
	v_mov_b32_e32 v41, v187
	v_mov_b32_e32 v47, v188
	v_mov_b32_e32 v49, v189
	v_pk_add_f32 v[34:35], v[38:39], v[40:41]
	v_pk_add_f32 v[36:37], v[46:47], v[48:49]
	s_nop 0
	v_pk_add_f32 v[34:35], v[34:35], v[36:37]
	s_nop 0
	v_pk_add_f32 v[38:39], v[34:35], v[34:35] op_sel:[0,1] op_sel_hi:[1,0]
	s_nop 1
	v_mov_b32_e32 v40, v191
	v_mov_b32_e32 v41, v192
	v_mov_b32_e32 v35, v193
	v_mov_b32_e32 v34, v190
	v_pk_add_f32 v[34:35], v[40:41], v[34:35]
	s_nop 0
	v_pk_add_f32 v[40:41], v[34:35], v[34:35] op_sel:[0,1] op_sel_hi:[1,0]
	s_nop 1
	v_add_f32_e32 v46, v194, v195
	v_add_f32_e32 v48, v196, v197
	s_nop 0
	v_mov_b32_e32 v39, v198
	v_mov_b32_e32 v41, v199
	v_mov_b32_e32 v47, v200
	v_mov_b32_e32 v49, v201
	v_pk_add_f32 v[34:35], v[38:39], v[40:41]
	v_pk_add_f32 v[36:37], v[46:47], v[48:49]
	s_nop 0
	v_pk_add_f32 v[34:35], v[34:35], v[36:37]
	v_lshlrev_b64 v[36:37], 10, v[42:43]
	v_add_f32_e32 v34, v34, v35
	v_fmamk_f32 v34, v34, 0x3a000000, v91
	v_rsq_f32_e32 v34, v34
	s_nop 0
	v_pk_mul_f32 v[30:31], v[30:31], v[34:35] op_sel_hi:[1,0]
	v_pk_mul_f32 v[38:39], v[28:29], v[34:35] op_sel_hi:[1,0]
	v_pk_mul_f32 v[28:29], v[26:27], v[34:35] op_sel_hi:[1,0]
	v_cvt_pk_bf16_f32 v26, v30, v31
	v_lshl_add_u64 v[30:31], s[54:55], 0, v[36:37]
	v_lshl_add_u64 v[30:31], v[30:31], 0, s[18:19]
	v_pk_mul_f32 v[32:33], v[32:33], v[34:35] op_sel_hi:[1,0]
	v_lshl_add_u64 v[30:31], v[30:31], 0, v[74:75]
	v_cvt_pk_bf16_f32 v27, v32, v33
	v_cvt_pk_bf16_f32 v28, v28, v29
	v_cvt_pk_bf16_f32 v29, v38, v39
	global_store_dwordx4 v[30:31], v[26:29], off
	v_pk_mul_f32 v[22:23], v[22:23], v[34:35] op_sel_hi:[1,0]
	v_pk_mul_f32 v[24:25], v[24:25], v[34:35] op_sel_hi:[1,0]
	v_pk_mul_f32 v[26:27], v[20:21], v[34:35] op_sel_hi:[1,0]
	v_pk_mul_f32 v[20:21], v[18:19], v[34:35] op_sel_hi:[1,0]
	v_cvt_pk_bf16_f32 v18, v22, v23
	v_cvt_pk_bf16_f32 v19, v24, v25
	s_nop 0
	v_cvt_pk_bf16_f32 v20, v20, v21
	v_cvt_pk_bf16_f32 v21, v26, v27
	global_store_dwordx4 v[30:31], v[18:21], off offset:256
	s_nop 1
	v_or_b32_e32 v18, 48, v84
	v_ashrrev_i32_e32 v19, 31, v18
	v_lshl_add_u64 v[28:29], v[18:19], 4, s[50:51]
	s_nop 0
	v_lshlrev_b64 v[18:19], 10, v[18:19]
	s_waitcnt vmcnt(6)
	v_mov_b32_e32 v30, v202
	v_mov_b32_e32 v31, v206
	v_mov_b32_e32 v24, v203
	v_mov_b32_e32 v25, v207
	v_pk_add_f32 v[20:21], v[30:31], v[24:25]
	v_mov_b32_e32 v24, v204
	v_mov_b32_e32 v25, v208
	v_mov_b32_e32 v26, v205
	v_mov_b32_e32 v27, v209
	v_pk_add_f32 v[22:23], v[24:25], v[26:27]
	s_nop 0
	v_pk_add_f32 v[20:21], v[20:21], v[22:23]
	s_nop 0
	v_add_f32_e32 v20, 0, v20
	v_add_f32_e32 v24, v20, v21
	s_nop 1
	v_mov_b32_e32 v26, v211
	v_mov_b32_e32 v27, v212
	v_mov_b32_e32 v21, v213
	v_mov_b32_e32 v20, v210
	v_pk_add_f32 v[20:21], v[26:27], v[20:21]
	s_nop 0
	v_pk_add_f32 v[26:27], v[20:21], v[20:21] op_sel:[0,1] op_sel_hi:[1,0]
	s_nop 1
	v_add_f32_e32 v30, v214, v215
	v_add_f32_e32 v32, v216, v217
	s_nop 0
	v_mov_b32_e32 v25, v218
	v_mov_b32_e32 v27, v219
	v_mov_b32_e32 v31, v220
	v_mov_b32_e32 v33, v221
	v_pk_add_f32 v[20:21], v[24:25], v[26:27]
	v_pk_add_f32 v[22:23], v[30:31], v[32:33]
	s_nop 0
	v_pk_add_f32 v[20:21], v[20:21], v[22:23]
	s_nop 0
	v_pk_add_f32 v[24:25], v[20:21], v[20:21] op_sel:[0,1] op_sel_hi:[1,0]
	s_nop 1
	v_mov_b32_e32 v26, v223
	v_mov_b32_e32 v27, v224
	v_mov_b32_e32 v21, v225
	v_mov_b32_e32 v20, v222
	v_pk_add_f32 v[20:21], v[26:27], v[20:21]
	s_nop 0
	v_pk_add_f32 v[26:27], v[20:21], v[20:21] op_sel:[0,1] op_sel_hi:[1,0]
	s_nop 1
	v_add_f32_e32 v30, v226, v227
	v_add_f32_e32 v32, v228, v229
	s_nop 0
	s_andn2_b64 vcc, exec, s[0:1]
	v_mov_b32_e32 v25, v230
	v_mov_b32_e32 v27, v231
	v_mov_b32_e32 v31, v232
	v_mov_b32_e32 v33, v233
	v_pk_add_f32 v[20:21], v[24:25], v[26:27]
	v_pk_add_f32 v[22:23], v[30:31], v[32:33]
	s_nop 0
	v_pk_add_f32 v[20:21], v[20:21], v[22:23]
	s_nop 0
	v_add_f32_e32 v20, v20, v21
	v_fmamk_f32 v20, v20, 0x3a000000, v91
	v_rsq_f32_e32 v20, v20
	s_nop 0
	v_pk_mul_f32 v[14:15], v[14:15], v[20:21] op_sel_hi:[1,0]
	v_pk_mul_f32 v[22:23], v[12:13], v[20:21] op_sel_hi:[1,0]
	v_pk_mul_f32 v[12:13], v[10:11], v[20:21] op_sel_hi:[1,0]
	v_cvt_pk_bf16_f32 v10, v14, v15
	v_lshl_add_u64 v[14:15], s[54:55], 0, v[18:19]
	v_lshl_add_u64 v[14:15], v[14:15], 0, s[18:19]
	v_pk_mul_f32 v[16:17], v[16:17], v[20:21] op_sel_hi:[1,0]
	v_lshl_add_u64 v[14:15], v[14:15], 0, v[74:75]
	v_cvt_pk_bf16_f32 v11, v16, v17
	v_cvt_pk_bf16_f32 v12, v12, v13
	v_cvt_pk_bf16_f32 v13, v22, v23
	global_store_dwordx4 v[14:15], v[10:13], off
	s_mov_b64 s[18:19], -1
	v_pk_mul_f32 v[8:9], v[8:9], v[20:21] op_sel_hi:[1,0]
	v_pk_mul_f32 v[10:11], v[4:5], v[20:21] op_sel_hi:[1,0]
	v_pk_mul_f32 v[4:5], v[2:3], v[20:21] op_sel_hi:[1,0]
	v_pk_mul_f32 v[6:7], v[6:7], v[20:21] op_sel_hi:[1,0]
	s_nop 0
	v_cvt_pk_bf16_f32 v2, v6, v7
	v_cvt_pk_bf16_f32 v3, v8, v9
	v_cvt_pk_bf16_f32 v4, v4, v5
	v_cvt_pk_bf16_f32 v5, v10, v11
	global_store_dwordx4 v[14:15], v[2:5], off offset:256
	s_cbranch_vccnz .LBB0_1662
	s_andn2_b64 vcc, exec, s[4:5]
	s_cbranch_vccnz .LBB0_1661
	s_barrier
	s_branch .LBB0_1661

.LBB0_2530:
	s_ashr_i32 s19, s18, 31
	v_readlane_b32 s60, v238, 13
	s_lshl_b64 s[22:23], s[18:19], 19
	v_readlane_b32 s72, v238, 25
	v_readlane_b32 s73, v238, 26
	s_add_u32 s22, s72, s22
	v_readlane_b32 s61, v238, 14
	v_readlane_b32 s62, v238, 15
	v_readlane_b32 s63, v238, 16
	v_readlane_b32 s64, v238, 17
	v_readlane_b32 s65, v238, 18
	v_readlane_b32 s66, v238, 19
	v_readlane_b32 s67, v238, 20
	v_readlane_b32 s68, v238, 21
	v_readlane_b32 s69, v238, 22
	v_readlane_b32 s70, v238, 23
	v_readlane_b32 s71, v238, 24
	v_readlane_b32 s74, v238, 27
	v_readlane_b32 s75, v238, 28
	s_addc_u32 s23, s73, s23
	s_and_b64 s[24:25], s[0:1], exec
	v_readlane_b32 s60, v237, 45
	s_cselect_b32 s5, s23, s7
	s_cselect_b32 s19, s22, s6
	s_ashr_i32 s21, s20, 31
	s_ashr_i32 s17, s16, 31
	v_readlane_b32 s66, v237, 51
	v_readlane_b32 s67, v237, 52
	s_lshl_b64 s[24:25], s[16:17], 19
	s_lshl_b64 s[36:37], s[20:21], 23
	s_mov_b64 s[54:55], s[66:67]
	s_add_u32 s17, s54, s36
	s_addc_u32 s21, s55, s37
	s_add_u32 s24, s17, s24
	s_addc_u32 s25, s21, s25
	s_and_b64 s[36:37], s[0:1], exec
	s_cselect_b32 s17, s25, s35
	s_cselect_b32 s21, s24, s34
	s_add_u32 s6, s6, 0x40080
	s_addc_u32 s7, s7, 0
	s_add_u32 s31, s34, 0x100
	s_addc_u32 s53, s35, 0
	v_readlane_b32 s98, v237, 31
	v_readlane_b32 s99, v237, 32
	v_lshl_or_b32 v239, s28, 7, v188
	v_lshlrev_b32_e32 v239, 2, v239
	v_lshl_add_u32 v239, s30, 14, v239
	s_add_u32 s100, s98, 0x2000
	s_addc_u32 s101, s99, 0
	s_nop 4
	global_load_dwordx4 v[240:243], v239, s[98:99]
	global_load_dwordx4 v[244:247], v239, s[98:99] offset:16
	global_load_dwordx4 v[248:251], v239, s[100:101]
	global_load_dwordx4 v[252:255], v239, s[100:101] offset:16
	s_mov_b32 s54, -2
	v_readlane_b32 s61, v237, 46
	v_readlane_b32 s62, v237, 47
	v_readlane_b32 s63, v237, 48
	v_readlane_b32 s64, v237, 49
	v_readlane_b32 s65, v237, 50
	v_readlane_b32 s68, v237, 53
	v_readlane_b32 s69, v237, 54
	v_readlane_b32 s70, v237, 55
	v_readlane_b32 s71, v237, 56
	v_readlane_b32 s72, v237, 57
	v_readlane_b32 s73, v237, 58
	v_readlane_b32 s74, v237, 59
	v_readlane_b32 s75, v237, 60

.LBB0_2534:
	s_ashr_i32 s31, s30, 31
	v_readlane_b32 s60, v237, 29
	s_lshl_b64 s[6:7], s[30:31], 14
	v_readlane_b32 s62, v237, 31
	v_lshl_or_b32 v18, s28, 7, v188
	v_readlane_b32 s63, v237, 32
	s_add_u32 s6, s62, s6
	s_addc_u32 s7, s63, s7
	v_ashrrev_i32_e32 v19, 31, v18
	s_nop 15
	s_nop 15
	s_nop 15
	s_lshl_b32 s5, s26, 8
	s_nop 0
	v_readlane_b32 s61, v237, 30
	v_readlane_b32 s64, v237, 33
	v_readlane_b32 s65, v237, 34
	v_readlane_b32 s66, v237, 35
	v_readlane_b32 s67, v237, 36
	v_readlane_b32 s68, v237, 37
	v_readlane_b32 s69, v237, 38
	v_readlane_b32 s70, v237, 39
	v_readlane_b32 s71, v237, 40
	v_readlane_b32 s72, v237, 41
	v_readlane_b32 s73, v237, 42
	v_readlane_b32 s74, v237, 43
	v_readlane_b32 s75, v237, 44
	v_readlane_b32 s60, v238, 13
	v_readlane_b32 s74, v238, 27
	v_readlane_b32 s75, v238, 28
	s_andn2_b64 vcc, exec, s[0:1]
	s_mov_b64 s[0:1], -1
	v_readlane_b32 s61, v238, 14
	v_readlane_b32 s62, v238, 15
	v_readlane_b32 s63, v238, 16
	v_readlane_b32 s64, v238, 17
	v_readlane_b32 s65, v238, 18
	v_readlane_b32 s66, v238, 19
	v_readlane_b32 s67, v238, 20
	v_readlane_b32 s68, v238, 21
	v_readlane_b32 s69, v238, 22
	v_readlane_b32 s70, v238, 23
	v_readlane_b32 s71, v238, 24
	v_readlane_b32 s72, v238, 25
	v_readlane_b32 s73, v238, 26
	v_fmamk_f32 v20, v158, 0x39800000, v240
	v_min_f32_e32 v20, 0x40e00000, v20
	v_mul_f32_e32 v28, 0xc01d265f, v20
	v_fmamk_f32 v21, v159, 0x39800000, v241
	v_min_f32_e32 v21, 0x40e00000, v21
	v_exp_f32_e32 v28, v28
	v_mul_f32_e32 v30, 0xc01d265f, v21
	v_exp_f32_e32 v30, v30
	v_add_f32_e32 v28, 1.0, v28
	v_rcp_f32_e32 v28, v28
	v_fmamk_f32 v27, v154, 0x39800000, v248
	v_fmamk_f32 v26, v148, 0x39800000, v246
	v_med3_f32 v27, v27, s50, v190
	v_add_f32_e32 v30, 1.0, v30
	v_min_f32_e32 v26, 0x40e00000, v26
	v_fma_f32 v27, v27, 4.0, 4.0
	v_rcp_f32_e32 v30, v30
	v_fmamk_f32 v29, v155, 0x39800000, v249
	v_mul_f32_e32 v20, v20, v28
	v_med3_f32 v29, v29, s50, v190
	v_mul_f32_e32 v27, v27, v20
	v_mul_f32_e32 v20, 0xc01d265f, v26
	v_fmamk_f32 v22, v160, 0x39800000, v242
	v_fma_f32 v29, v29, 4.0, 4.0
	v_exp_f32_e32 v20, v20
	v_fmamk_f32 v23, v161, 0x39800000, v243
	v_fmamk_f32 v24, v146, 0x39800000, v244
	v_fmamk_f32 v25, v147, 0x39800000, v245
	v_min_f32_e32 v22, 0x40e00000, v22
	v_mul_f32_e32 v21, v21, v30
	v_min_f32_e32 v23, 0x40e00000, v23
	v_min_f32_e32 v24, 0x40e00000, v24
	v_min_f32_e32 v25, 0x40e00000, v25
	v_mul_f32_e32 v32, 0xc01d265f, v22
	v_mul_f32_e32 v21, v29, v21
	v_fmamk_f32 v29, v149, 0x39800000, v247
	v_mul_f32_e32 v146, 0xc01d265f, v23
	v_fmamk_f32 v147, v150, 0x39800000, v252
	v_mul_f32_e32 v148, 0xc01d265f, v24
	v_fmamk_f32 v150, v151, 0x39800000, v253
	v_mul_f32_e32 v151, 0xc01d265f, v25
	v_min_f32_e32 v29, 0x40e00000, v29
	v_exp_f32_e32 v32, v32
	v_add_f32_e32 v20, 1.0, v20
	v_mul_f32_e32 v30, 0xc01d265f, v29
	v_exp_f32_e32 v146, v146
	v_exp_f32_e32 v148, v148
	v_exp_f32_e32 v151, v151
	v_rcp_f32_e32 v20, v20
	v_fmamk_f32 v152, v152, 0x39800000, v254
	v_exp_f32_e32 v30, v30
	v_med3_f32 v28, v152, s50, v190
	v_add_f32_e32 v32, 1.0, v32
	v_fma_f32 v28, v28, 4.0, 4.0
	v_add_f32_e32 v146, 1.0, v146
	v_add_f32_e32 v148, 1.0, v148
	v_add_f32_e32 v151, 1.0, v151
	v_rcp_f32_e32 v32, v32
	v_mul_f32_e32 v20, v26, v20
	v_fmamk_f32 v31, v156, 0x39800000, v250
	v_rcp_f32_e32 v146, v146
	v_rcp_f32_e32 v148, v148
	v_rcp_f32_e32 v151, v151
	v_mul_f32_e32 v26, v28, v20
	v_add_f32_e32 v28, 1.0, v30
	v_fmamk_f32 v33, v157, 0x39800000, v251
	v_med3_f32 v31, v31, s50, v190
	v_rcp_f32_e32 v28, v28
	v_med3_f32 v33, v33, s50, v190
	v_med3_f32 v147, v147, s50, v190
	v_med3_f32 v150, v150, s50, v190
	v_fma_f32 v31, v31, 4.0, 4.0
	v_fma_f32 v33, v33, 4.0, 4.0
	v_fma_f32 v147, v147, 4.0, 4.0
	v_fma_f32 v150, v150, 4.0, 4.0
	v_mul_f32_e32 v22, v22, v32
	v_mul_f32_e32 v23, v23, v146
	v_mul_f32_e32 v24, v24, v148
	v_mul_f32_e32 v25, v25, v151
	v_mul_f32_e32 v22, v31, v22
	v_mul_f32_e32 v23, v33, v23
	v_mul_f32_e32 v24, v147, v24
	v_mul_f32_e32 v25, v150, v25
	v_fmamk_f32 v20, v153, 0x39800000, v255
	v_mul_f32_e32 v28, v29, v28
	v_mov_b32_e32 v29, v22
	v_med3_f32 v20, v20, s50, v190
	v_mov_b32_e32 v30, v23
	v_cvt_pk_fp8_f32 v22, v27, v21
	v_mov_b32_e32 v21, v24
	v_mov_b32_e32 v24, v25
	v_fma_f32 v20, v20, 4.0, 4.0
	v_cvt_pk_fp8_f32 v23, v21, v24
	v_mul_f32_e32 v28, v20, v28
	v_add_u32_e32 v20, s5, v1
	v_mov_b32_e32 v21, v26
	v_mov_b32_e32 v24, v28
	v_cvt_pk_fp8_f32 v22, v29, v30 op_sel:[0,0,1]
	v_cvt_pk_fp8_f32 v23, v21, v24 op_sel:[0,0,1]
	v_ashrrev_i32_e32 v21, 31, v20
	v_lshlrev_b64 v[24:25], 11, v[20:21]
	v_lshl_add_u64 v[24:25], s[74:75], 0, v[24:25]
	v_fmamk_f32 v21, v138, 0x39800000, v240
	v_lshl_add_u64 v[24:25], v[24:25], 0, v[18:19]
	v_min_f32_e32 v21, 0x40e00000, v21
	global_store_dwordx2 v[24:25], v[22:23], off
	v_mul_f32_e32 v23, 0xc01d265f, v21
	v_exp_f32_e32 v23, v23
	v_fmamk_f32 v24, v139, 0x39800000, v241
	v_min_f32_e32 v24, 0x40e00000, v24
	v_mul_f32_e32 v25, 0xc01d265f, v24
	v_add_f32_e32 v23, 1.0, v23
	v_rcp_f32_e32 v23, v23
	v_exp_f32_e32 v25, v25
	v_fmamk_f32 v22, v142, 0x39800000, v248
	v_med3_f32 v22, v22, s50, v190
	v_fma_f32 v22, v22, 4.0, 4.0
	v_mul_f32_e32 v21, v21, v23
	v_add_f32_e32 v23, 1.0, v25
	v_rcp_f32_e32 v23, v23
	v_mul_f32_e32 v21, v22, v21
	v_fmamk_f32 v22, v143, 0x39800000, v249
	v_med3_f32 v22, v22, s50, v190
	v_fma_f32 v22, v22, 4.0, 4.0
	v_mul_f32_e32 v23, v24, v23
	v_mul_f32_e32 v23, v22, v23
	v_fmamk_f32 v22, v140, 0x39800000, v242
	v_min_f32_e32 v22, 0x40e00000, v22
	v_mul_f32_e32 v25, 0xc01d265f, v22
	v_exp_f32_e32 v25, v25
	v_fmamk_f32 v26, v141, 0x39800000, v243
	v_min_f32_e32 v26, 0x40e00000, v26
	v_mul_f32_e32 v27, 0xc01d265f, v26
	v_add_f32_e32 v25, 1.0, v25
	v_rcp_f32_e32 v25, v25
	v_exp_f32_e32 v27, v27
	v_fmamk_f32 v24, v144, 0x39800000, v250
	v_med3_f32 v24, v24, s50, v190
	v_fma_f32 v24, v24, 4.0, 4.0
	v_mul_f32_e32 v22, v22, v25
	v_add_f32_e32 v25, 1.0, v27
	v_rcp_f32_e32 v25, v25
	v_mul_f32_e32 v24, v24, v22
	v_fmamk_f32 v22, v145, 0x39800000, v251
	v_med3_f32 v22, v22, s50, v190
	v_fma_f32 v22, v22, 4.0, 4.0
	v_mul_f32_e32 v25, v26, v25
	v_mul_f32_e32 v25, v22, v25
	v_fmamk_f32 v22, v130, 0x39800000, v244
	v_min_f32_e32 v22, 0x40e00000, v22
	v_mul_f32_e32 v27, 0xc01d265f, v22
	v_exp_f32_e32 v27, v27
	v_fmamk_f32 v28, v131, 0x39800000, v245
	v_min_f32_e32 v28, 0x40e00000, v28
	v_mul_f32_e32 v29, 0xc01d265f, v28
	v_add_f32_e32 v27, 1.0, v27
	v_rcp_f32_e32 v27, v27
	v_exp_f32_e32 v29, v29
	v_fmamk_f32 v26, v134, 0x39800000, v252
	v_med3_f32 v26, v26, s50, v190
	v_fma_f32 v26, v26, 4.0, 4.0
	v_mul_f32_e32 v22, v22, v27
	v_add_f32_e32 v27, 1.0, v29
	v_rcp_f32_e32 v27, v27
	v_mul_f32_e32 v26, v26, v22
	v_fmamk_f32 v22, v135, 0x39800000, v253
	v_med3_f32 v22, v22, s50, v190
	v_fma_f32 v22, v22, 4.0, 4.0
	v_mul_f32_e32 v27, v28, v27
	v_mul_f32_e32 v27, v22, v27
	v_fmamk_f32 v22, v132, 0x39800000, v246
	v_min_f32_e32 v22, 0x40e00000, v22
	v_mul_f32_e32 v29, 0xc01d265f, v22
	v_exp_f32_e32 v29, v29
	v_fmamk_f32 v30, v133, 0x39800000, v247
	v_min_f32_e32 v30, 0x40e00000, v30
	v_mul_f32_e32 v31, 0xc01d265f, v30
	v_add_f32_e32 v29, 1.0, v29
	v_rcp_f32_e32 v29, v29
	v_exp_f32_e32 v31, v31
	v_fmamk_f32 v28, v136, 0x39800000, v254
	v_med3_f32 v28, v28, s50, v190
	v_mul_f32_e32 v22, v22, v29
	v_add_f32_e32 v29, 1.0, v31
	v_rcp_f32_e32 v29, v29
	v_fma_f32 v28, v28, 4.0, 4.0
	v_mul_f32_e32 v28, v28, v22
	v_fmamk_f32 v22, v137, 0x39800000, v255
	v_mul_f32_e32 v29, v30, v29
	v_mov_b32_e32 v30, v24
	v_med3_f32 v22, v22, s50, v190
	v_mov_b32_e32 v31, v25
	v_cvt_pk_fp8_f32 v24, v21, v23
	v_mov_b32_e32 v21, v26
	v_mov_b32_e32 v23, v27
	v_fma_f32 v22, v22, 4.0, 4.0
	v_cvt_pk_fp8_f32 v25, v21, v23
	v_mul_f32_e32 v29, v22, v29
	v_add_u32_e32 v22, s5, v185
	v_mov_b32_e32 v21, v28
	v_mov_b32_e32 v23, v29
	v_cvt_pk_fp8_f32 v24, v30, v31 op_sel:[0,0,1]
	v_cvt_pk_fp8_f32 v25, v21, v23 op_sel:[0,0,1]
	v_ashrrev_i32_e32 v23, 31, v22
	v_lshlrev_b64 v[22:23], 11, v[22:23]
	v_lshl_add_u64 v[22:23], s[74:75], 0, v[22:23]
	v_fmamk_f32 v21, v122, 0x39800000, v240
	v_lshl_add_u64 v[22:23], v[22:23], 0, v[18:19]
	v_min_f32_e32 v21, 0x40e00000, v21
	global_store_dwordx2 v[22:23], v[24:25], off
	v_mul_f32_e32 v23, 0xc01d265f, v21
	v_exp_f32_e32 v23, v23
	v_fmamk_f32 v24, v123, 0x39800000, v241
	v_min_f32_e32 v24, 0x40e00000, v24
	v_mul_f32_e32 v25, 0xc01d265f, v24
	v_add_f32_e32 v23, 1.0, v23
	v_rcp_f32_e32 v23, v23
	v_exp_f32_e32 v25, v25
	v_fmamk_f32 v22, v126, 0x39800000, v248
	v_med3_f32 v22, v22, s50, v190
	v_fma_f32 v22, v22, 4.0, 4.0
	v_mul_f32_e32 v21, v21, v23
	v_add_f32_e32 v23, 1.0, v25
	v_rcp_f32_e32 v23, v23
	v_mul_f32_e32 v21, v22, v21
	v_fmamk_f32 v22, v127, 0x39800000, v249
	v_med3_f32 v22, v22, s50, v190
	v_fma_f32 v22, v22, 4.0, 4.0
	v_mul_f32_e32 v23, v24, v23
	v_mul_f32_e32 v23, v22, v23
	v_fmamk_f32 v22, v124, 0x39800000, v242
	v_min_f32_e32 v22, 0x40e00000, v22
	v_mul_f32_e32 v25, 0xc01d265f, v22
	v_exp_f32_e32 v25, v25
	v_fmamk_f32 v26, v125, 0x39800000, v243
	v_min_f32_e32 v26, 0x40e00000, v26
	v_mul_f32_e32 v27, 0xc01d265f, v26
	v_add_f32_e32 v25, 1.0, v25
	v_rcp_f32_e32 v25, v25
	v_exp_f32_e32 v27, v27
	v_fmamk_f32 v24, v128, 0x39800000, v250
	v_med3_f32 v24, v24, s50, v190
	v_fma_f32 v24, v24, 4.0, 4.0
	v_mul_f32_e32 v22, v22, v25
	v_add_f32_e32 v25, 1.0, v27
	v_rcp_f32_e32 v25, v25
	v_mul_f32_e32 v24, v24, v22
	v_fmamk_f32 v22, v129, 0x39800000, v251
	v_med3_f32 v22, v22, s50, v190
	v_fma_f32 v22, v22, 4.0, 4.0
	v_mul_f32_e32 v25, v26, v25
	v_mul_f32_e32 v25, v22, v25
	v_fmamk_f32 v22, v114, 0x39800000, v244
	v_min_f32_e32 v22, 0x40e00000, v22
	v_mul_f32_e32 v27, 0xc01d265f, v22
	v_exp_f32_e32 v27, v27
	v_fmamk_f32 v28, v115, 0x39800000, v245
	v_min_f32_e32 v28, 0x40e00000, v28
	v_mul_f32_e32 v29, 0xc01d265f, v28
	v_add_f32_e32 v27, 1.0, v27
	v_rcp_f32_e32 v27, v27
	v_exp_f32_e32 v29, v29
	v_fmamk_f32 v26, v118, 0x39800000, v252
	v_med3_f32 v26, v26, s50, v190
	v_fma_f32 v26, v26, 4.0, 4.0
	v_mul_f32_e32 v22, v22, v27
	v_add_f32_e32 v27, 1.0, v29
	v_rcp_f32_e32 v27, v27
	v_mul_f32_e32 v26, v26, v22
	v_fmamk_f32 v22, v119, 0x39800000, v253
	v_med3_f32 v22, v22, s50, v190
	v_fma_f32 v22, v22, 4.0, 4.0
	v_mul_f32_e32 v27, v28, v27
	v_mul_f32_e32 v27, v22, v27
	v_fmamk_f32 v22, v116, 0x39800000, v246
	v_min_f32_e32 v22, 0x40e00000, v22
	v_mul_f32_e32 v29, 0xc01d265f, v22
	v_exp_f32_e32 v29, v29
	v_fmamk_f32 v30, v117, 0x39800000, v247
	v_min_f32_e32 v30, 0x40e00000, v30
	v_mul_f32_e32 v31, 0xc01d265f, v30
	v_add_f32_e32 v29, 1.0, v29
	v_rcp_f32_e32 v29, v29
	v_exp_f32_e32 v31, v31
	v_fmamk_f32 v28, v120, 0x39800000, v254
	v_med3_f32 v28, v28, s50, v190
	v_mul_f32_e32 v22, v22, v29
	v_add_f32_e32 v29, 1.0, v31
	v_rcp_f32_e32 v29, v29
	v_fma_f32 v28, v28, 4.0, 4.0
	v_mul_f32_e32 v28, v28, v22
	v_fmamk_f32 v22, v121, 0x39800000, v255
	v_mul_f32_e32 v29, v30, v29
	v_mov_b32_e32 v30, v24
	v_med3_f32 v22, v22, s50, v190
	v_mov_b32_e32 v31, v25
	v_cvt_pk_fp8_f32 v24, v21, v23
	v_mov_b32_e32 v21, v26
	v_mov_b32_e32 v23, v27
	v_fma_f32 v22, v22, 4.0, 4.0
	v_cvt_pk_fp8_f32 v25, v21, v23
	v_mul_f32_e32 v29, v22, v29
	v_add_u32_e32 v22, s5, v186
	v_mov_b32_e32 v21, v28
	v_mov_b32_e32 v23, v29
	v_cvt_pk_fp8_f32 v24, v30, v31 op_sel:[0,0,1]
	v_cvt_pk_fp8_f32 v25, v21, v23 op_sel:[0,0,1]
	v_ashrrev_i32_e32 v23, 31, v22
	v_lshlrev_b64 v[22:23], 11, v[22:23]
	v_lshl_add_u64 v[22:23], s[74:75], 0, v[22:23]
	v_fmamk_f32 v21, v106, 0x39800000, v240
	v_lshl_add_u64 v[22:23], v[22:23], 0, v[18:19]
	v_min_f32_e32 v21, 0x40e00000, v21
	global_store_dwordx2 v[22:23], v[24:25], off
	v_mul_f32_e32 v23, 0xc01d265f, v21
	v_exp_f32_e32 v23, v23
	v_fmamk_f32 v24, v107, 0x39800000, v241
	v_min_f32_e32 v24, 0x40e00000, v24
	v_mul_f32_e32 v25, 0xc01d265f, v24
	v_add_f32_e32 v23, 1.0, v23
	v_rcp_f32_e32 v23, v23
	v_exp_f32_e32 v25, v25
	v_fmamk_f32 v22, v110, 0x39800000, v248
	v_med3_f32 v22, v22, s50, v190
	v_fma_f32 v22, v22, 4.0, 4.0
	v_mul_f32_e32 v21, v21, v23
	v_add_f32_e32 v23, 1.0, v25
	v_rcp_f32_e32 v23, v23
	v_mul_f32_e32 v21, v22, v21
	v_fmamk_f32 v22, v111, 0x39800000, v249
	v_med3_f32 v22, v22, s50, v190
	v_fma_f32 v22, v22, 4.0, 4.0
	v_mul_f32_e32 v23, v24, v23
	v_mul_f32_e32 v23, v22, v23
	v_fmamk_f32 v22, v108, 0x39800000, v242
	v_min_f32_e32 v22, 0x40e00000, v22
	v_mul_f32_e32 v25, 0xc01d265f, v22
	v_exp_f32_e32 v25, v25
	v_fmamk_f32 v26, v109, 0x39800000, v243
	v_min_f32_e32 v26, 0x40e00000, v26
	v_mul_f32_e32 v27, 0xc01d265f, v26
	v_add_f32_e32 v25, 1.0, v25
	v_rcp_f32_e32 v25, v25
	v_exp_f32_e32 v27, v27
	v_fmamk_f32 v24, v112, 0x39800000, v250
	v_med3_f32 v24, v24, s50, v190
	v_fma_f32 v24, v24, 4.0, 4.0
	v_mul_f32_e32 v22, v22, v25
	v_add_f32_e32 v25, 1.0, v27
	v_rcp_f32_e32 v25, v25
	v_mul_f32_e32 v24, v24, v22
	v_fmamk_f32 v22, v113, 0x39800000, v251
	v_med3_f32 v22, v22, s50, v190
	v_fma_f32 v22, v22, 4.0, 4.0
	v_mul_f32_e32 v25, v26, v25
	v_mul_f32_e32 v25, v22, v25
	v_fmamk_f32 v22, v98, 0x39800000, v244
	v_min_f32_e32 v22, 0x40e00000, v22
	v_mul_f32_e32 v27, 0xc01d265f, v22
	v_exp_f32_e32 v27, v27
	v_fmamk_f32 v28, v99, 0x39800000, v245
	v_min_f32_e32 v28, 0x40e00000, v28
	v_mul_f32_e32 v29, 0xc01d265f, v28
	v_add_f32_e32 v27, 1.0, v27
	v_rcp_f32_e32 v27, v27
	v_exp_f32_e32 v29, v29
	v_fmamk_f32 v26, v102, 0x39800000, v252
	v_med3_f32 v26, v26, s50, v190
	v_fma_f32 v26, v26, 4.0, 4.0
	v_mul_f32_e32 v22, v22, v27
	v_add_f32_e32 v27, 1.0, v29
	v_rcp_f32_e32 v27, v27
	v_mul_f32_e32 v26, v26, v22
	v_fmamk_f32 v22, v103, 0x39800000, v253
	v_med3_f32 v22, v22, s50, v190
	v_fma_f32 v22, v22, 4.0, 4.0
	v_mul_f32_e32 v27, v28, v27
	v_mul_f32_e32 v27, v22, v27
	v_fmamk_f32 v22, v100, 0x39800000, v246
	v_min_f32_e32 v22, 0x40e00000, v22
	v_mul_f32_e32 v29, 0xc01d265f, v22
	v_exp_f32_e32 v29, v29
	v_fmamk_f32 v30, v101, 0x39800000, v247
	v_min_f32_e32 v30, 0x40e00000, v30
	v_mul_f32_e32 v31, 0xc01d265f, v30
	v_add_f32_e32 v29, 1.0, v29
	v_rcp_f32_e32 v29, v29
	v_exp_f32_e32 v31, v31
	v_fmamk_f32 v28, v104, 0x39800000, v254
	v_med3_f32 v28, v28, s50, v190
	v_mul_f32_e32 v22, v22, v29
	v_add_f32_e32 v29, 1.0, v31
	v_rcp_f32_e32 v29, v29
	v_fma_f32 v28, v28, 4.0, 4.0
	v_mul_f32_e32 v28, v28, v22
	v_fmamk_f32 v22, v105, 0x39800000, v255
	v_mul_f32_e32 v29, v30, v29
	v_mov_b32_e32 v30, v24
	v_med3_f32 v22, v22, s50, v190
	v_mov_b32_e32 v31, v25
	v_cvt_pk_fp8_f32 v24, v21, v23
	v_mov_b32_e32 v21, v26
	v_mov_b32_e32 v23, v27
	v_fma_f32 v22, v22, 4.0, 4.0
	v_cvt_pk_fp8_f32 v25, v21, v23
	v_mul_f32_e32 v29, v22, v29
	v_add_u32_e32 v22, s5, v187
	v_mov_b32_e32 v21, v28
	v_mov_b32_e32 v23, v29
	v_cvt_pk_fp8_f32 v24, v30, v31 op_sel:[0,0,1]
	v_cvt_pk_fp8_f32 v25, v21, v23 op_sel:[0,0,1]
	v_ashrrev_i32_e32 v23, 31, v22
	v_lshlrev_b64 v[22:23], 11, v[22:23]
	v_lshl_add_u64 v[22:23], s[74:75], 0, v[22:23]
	v_fmamk_f32 v21, v90, 0x39800000, v240
	v_lshl_add_u64 v[22:23], v[22:23], 0, v[18:19]
	v_min_f32_e32 v21, 0x40e00000, v21
	global_store_dwordx2 v[22:23], v[24:25], off
	v_mul_f32_e32 v23, 0xc01d265f, v21
	v_exp_f32_e32 v23, v23
	v_fmamk_f32 v24, v91, 0x39800000, v241
	v_min_f32_e32 v24, 0x40e00000, v24
	v_mul_f32_e32 v25, 0xc01d265f, v24
	v_add_f32_e32 v23, 1.0, v23
	v_rcp_f32_e32 v23, v23
	v_exp_f32_e32 v25, v25
	v_fmamk_f32 v22, v94, 0x39800000, v248
	v_med3_f32 v22, v22, s50, v190
	v_fma_f32 v22, v22, 4.0, 4.0
	v_mul_f32_e32 v21, v21, v23
	v_add_f32_e32 v23, 1.0, v25
	v_rcp_f32_e32 v23, v23
	v_mul_f32_e32 v21, v22, v21
	v_fmamk_f32 v22, v95, 0x39800000, v249
	v_med3_f32 v22, v22, s50, v190
	v_fma_f32 v22, v22, 4.0, 4.0
	v_mul_f32_e32 v23, v24, v23
	v_mul_f32_e32 v23, v22, v23
	v_fmamk_f32 v22, v92, 0x39800000, v242
	v_min_f32_e32 v22, 0x40e00000, v22
	v_mul_f32_e32 v25, 0xc01d265f, v22
	v_exp_f32_e32 v25, v25
	v_fmamk_f32 v26, v93, 0x39800000, v243
	v_min_f32_e32 v26, 0x40e00000, v26
	v_mul_f32_e32 v27, 0xc01d265f, v26
	v_add_f32_e32 v25, 1.0, v25
	v_rcp_f32_e32 v25, v25
	v_exp_f32_e32 v27, v27
	v_fmamk_f32 v24, v96, 0x39800000, v250
	v_med3_f32 v24, v24, s50, v190
	v_fma_f32 v24, v24, 4.0, 4.0
	v_mul_f32_e32 v22, v22, v25
	v_add_f32_e32 v25, 1.0, v27
	v_rcp_f32_e32 v25, v25
	v_mul_f32_e32 v24, v24, v22
	v_fmamk_f32 v22, v97, 0x39800000, v251
	v_med3_f32 v22, v22, s50, v190
	v_fma_f32 v22, v22, 4.0, 4.0
	v_mul_f32_e32 v25, v26, v25
	v_mul_f32_e32 v25, v22, v25
	v_fmamk_f32 v22, v82, 0x39800000, v244
	v_min_f32_e32 v22, 0x40e00000, v22
	v_mul_f32_e32 v27, 0xc01d265f, v22
	v_exp_f32_e32 v27, v27
	v_fmamk_f32 v28, v83, 0x39800000, v245
	v_min_f32_e32 v28, 0x40e00000, v28
	v_mul_f32_e32 v29, 0xc01d265f, v28
	v_add_f32_e32 v27, 1.0, v27
	v_rcp_f32_e32 v27, v27
	v_exp_f32_e32 v29, v29
	v_fmamk_f32 v26, v86, 0x39800000, v252
	v_med3_f32 v26, v26, s50, v190
	v_fma_f32 v26, v26, 4.0, 4.0
	v_mul_f32_e32 v22, v22, v27
	v_add_f32_e32 v27, 1.0, v29
	v_rcp_f32_e32 v27, v27
	v_mul_f32_e32 v26, v26, v22
	v_fmamk_f32 v22, v87, 0x39800000, v253
	v_med3_f32 v22, v22, s50, v190
	v_fma_f32 v22, v22, 4.0, 4.0
	v_mul_f32_e32 v27, v28, v27
	v_mul_f32_e32 v27, v22, v27
	v_fmamk_f32 v22, v84, 0x39800000, v246
	v_min_f32_e32 v22, 0x40e00000, v22
	v_mul_f32_e32 v29, 0xc01d265f, v22
	v_exp_f32_e32 v29, v29
	v_fmamk_f32 v30, v85, 0x39800000, v247
	v_min_f32_e32 v30, 0x40e00000, v30
	v_mul_f32_e32 v31, 0xc01d265f, v30
	v_add_f32_e32 v29, 1.0, v29
	v_rcp_f32_e32 v29, v29
	v_exp_f32_e32 v31, v31
	v_fmamk_f32 v28, v88, 0x39800000, v254
	v_med3_f32 v28, v28, s50, v190
	v_mul_f32_e32 v22, v22, v29
	v_add_f32_e32 v29, 1.0, v31
	v_rcp_f32_e32 v29, v29
	v_fma_f32 v28, v28, 4.0, 4.0
	v_mul_f32_e32 v28, v28, v22
	v_fmamk_f32 v22, v89, 0x39800000, v255
	v_mul_f32_e32 v29, v30, v29
	v_mov_b32_e32 v30, v24
	v_med3_f32 v22, v22, s50, v190
	v_mov_b32_e32 v31, v25
	v_cvt_pk_fp8_f32 v24, v21, v23
	v_mov_b32_e32 v21, v26
	v_mov_b32_e32 v23, v27
	v_fma_f32 v22, v22, 4.0, 4.0
	v_cvt_pk_fp8_f32 v25, v21, v23
	v_mul_f32_e32 v29, v22, v29
	v_add_u32_e32 v22, 0x80, v20
	v_mov_b32_e32 v21, v28
	v_mov_b32_e32 v23, v29
	v_cvt_pk_fp8_f32 v24, v30, v31 op_sel:[0,0,1]
	v_cvt_pk_fp8_f32 v25, v21, v23 op_sel:[0,0,1]
	v_ashrrev_i32_e32 v23, 31, v22
	v_lshlrev_b64 v[22:23], 11, v[22:23]
	v_lshl_add_u64 v[22:23], s[74:75], 0, v[22:23]
	v_fmamk_f32 v21, v74, 0x39800000, v240
	v_lshl_add_u64 v[22:23], v[22:23], 0, v[18:19]
	v_min_f32_e32 v21, 0x40e00000, v21
	global_store_dwordx2 v[22:23], v[24:25], off
	v_mul_f32_e32 v23, 0xc01d265f, v21
	v_exp_f32_e32 v23, v23
	v_fmamk_f32 v24, v75, 0x39800000, v241
	v_min_f32_e32 v24, 0x40e00000, v24
	v_mul_f32_e32 v25, 0xc01d265f, v24
	v_add_f32_e32 v23, 1.0, v23
	v_rcp_f32_e32 v23, v23
	v_exp_f32_e32 v25, v25
	v_fmamk_f32 v22, v78, 0x39800000, v248
	v_med3_f32 v22, v22, s50, v190
	v_fma_f32 v22, v22, 4.0, 4.0
	v_mul_f32_e32 v21, v21, v23
	v_add_f32_e32 v23, 1.0, v25
	v_rcp_f32_e32 v23, v23
	v_mul_f32_e32 v21, v22, v21
	v_fmamk_f32 v22, v79, 0x39800000, v249
	v_med3_f32 v22, v22, s50, v190
	v_fma_f32 v22, v22, 4.0, 4.0
	v_mul_f32_e32 v23, v24, v23
	v_mul_f32_e32 v23, v22, v23
	v_fmamk_f32 v22, v76, 0x39800000, v242
	v_min_f32_e32 v22, 0x40e00000, v22
	v_mul_f32_e32 v25, 0xc01d265f, v22
	v_exp_f32_e32 v25, v25
	v_fmamk_f32 v26, v77, 0x39800000, v243
	v_min_f32_e32 v26, 0x40e00000, v26
	v_mul_f32_e32 v27, 0xc01d265f, v26
	v_add_f32_e32 v25, 1.0, v25
	v_rcp_f32_e32 v25, v25
	v_exp_f32_e32 v27, v27
	v_fmamk_f32 v24, v80, 0x39800000, v250
	v_med3_f32 v24, v24, s50, v190
	v_fma_f32 v24, v24, 4.0, 4.0
	v_mul_f32_e32 v22, v22, v25
	v_add_f32_e32 v25, 1.0, v27
	v_rcp_f32_e32 v25, v25
	v_mul_f32_e32 v24, v24, v22
	v_fmamk_f32 v22, v81, 0x39800000, v251
	v_med3_f32 v22, v22, s50, v190
	v_fma_f32 v22, v22, 4.0, 4.0
	v_mul_f32_e32 v25, v26, v25
	v_mul_f32_e32 v25, v22, v25
	v_fmamk_f32 v22, v66, 0x39800000, v244
	v_min_f32_e32 v22, 0x40e00000, v22
	v_mul_f32_e32 v27, 0xc01d265f, v22
	v_exp_f32_e32 v27, v27
	v_fmamk_f32 v28, v67, 0x39800000, v245
	v_min_f32_e32 v28, 0x40e00000, v28
	v_mul_f32_e32 v29, 0xc01d265f, v28
	v_add_f32_e32 v27, 1.0, v27
	v_rcp_f32_e32 v27, v27
	v_exp_f32_e32 v29, v29
	v_fmamk_f32 v26, v70, 0x39800000, v252
	v_med3_f32 v26, v26, s50, v190
	v_fma_f32 v26, v26, 4.0, 4.0
	v_mul_f32_e32 v22, v22, v27
	v_add_f32_e32 v27, 1.0, v29
	v_rcp_f32_e32 v27, v27
	v_mul_f32_e32 v26, v26, v22
	v_fmamk_f32 v22, v71, 0x39800000, v253
	v_med3_f32 v22, v22, s50, v190
	v_fma_f32 v22, v22, 4.0, 4.0
	v_mul_f32_e32 v27, v28, v27
	v_mul_f32_e32 v27, v22, v27
	v_fmamk_f32 v22, v68, 0x39800000, v246
	v_min_f32_e32 v22, 0x40e00000, v22
	v_mul_f32_e32 v29, 0xc01d265f, v22
	v_exp_f32_e32 v29, v29
	v_fmamk_f32 v30, v69, 0x39800000, v247
	v_min_f32_e32 v30, 0x40e00000, v30
	v_mul_f32_e32 v31, 0xc01d265f, v30
	v_add_f32_e32 v29, 1.0, v29
	v_rcp_f32_e32 v29, v29
	v_exp_f32_e32 v31, v31
	v_fmamk_f32 v28, v72, 0x39800000, v254
	v_med3_f32 v28, v28, s50, v190
	v_mul_f32_e32 v22, v22, v29
	v_add_f32_e32 v29, 1.0, v31
	v_rcp_f32_e32 v29, v29
	v_fma_f32 v28, v28, 4.0, 4.0
	v_mul_f32_e32 v28, v28, v22
	v_fmamk_f32 v22, v73, 0x39800000, v255
	v_mul_f32_e32 v29, v30, v29
	v_mov_b32_e32 v30, v24
	v_med3_f32 v22, v22, s50, v190
	v_mov_b32_e32 v31, v25
	v_cvt_pk_fp8_f32 v24, v21, v23
	v_mov_b32_e32 v21, v26
	v_mov_b32_e32 v23, v27
	v_fma_f32 v22, v22, 4.0, 4.0
	v_cvt_pk_fp8_f32 v25, v21, v23
	v_mul_f32_e32 v29, v22, v29
	v_add_u32_e32 v22, 0x90, v20
	v_mov_b32_e32 v21, v28
	v_mov_b32_e32 v23, v29
	v_cvt_pk_fp8_f32 v24, v30, v31 op_sel:[0,0,1]
	v_cvt_pk_fp8_f32 v25, v21, v23 op_sel:[0,0,1]
	v_ashrrev_i32_e32 v23, 31, v22
	v_lshlrev_b64 v[22:23], 11, v[22:23]
	v_lshl_add_u64 v[22:23], s[74:75], 0, v[22:23]
	v_fmamk_f32 v21, v58, 0x39800000, v240
	v_lshl_add_u64 v[22:23], v[22:23], 0, v[18:19]
	v_min_f32_e32 v21, 0x40e00000, v21
	global_store_dwordx2 v[22:23], v[24:25], off
	v_mul_f32_e32 v23, 0xc01d265f, v21
	v_exp_f32_e32 v23, v23
	v_fmamk_f32 v24, v59, 0x39800000, v241
	v_min_f32_e32 v24, 0x40e00000, v24
	v_mul_f32_e32 v25, 0xc01d265f, v24
	v_add_f32_e32 v23, 1.0, v23
	v_rcp_f32_e32 v23, v23
	v_exp_f32_e32 v25, v25
	v_fmamk_f32 v22, v62, 0x39800000, v248
	v_med3_f32 v22, v22, s50, v190
	v_fma_f32 v22, v22, 4.0, 4.0
	v_mul_f32_e32 v21, v21, v23
	v_add_f32_e32 v23, 1.0, v25
	v_rcp_f32_e32 v23, v23
	v_mul_f32_e32 v21, v22, v21
	v_fmamk_f32 v22, v63, 0x39800000, v249
	v_med3_f32 v22, v22, s50, v190
	v_fma_f32 v22, v22, 4.0, 4.0
	v_mul_f32_e32 v23, v24, v23
	v_mul_f32_e32 v23, v22, v23
	v_fmamk_f32 v22, v60, 0x39800000, v242
	v_min_f32_e32 v22, 0x40e00000, v22
	v_mul_f32_e32 v25, 0xc01d265f, v22
	v_exp_f32_e32 v25, v25
	v_fmamk_f32 v26, v61, 0x39800000, v243
	v_min_f32_e32 v26, 0x40e00000, v26
	v_mul_f32_e32 v27, 0xc01d265f, v26
	v_add_f32_e32 v25, 1.0, v25
	v_rcp_f32_e32 v25, v25
	v_exp_f32_e32 v27, v27
	v_fmamk_f32 v24, v64, 0x39800000, v250
	v_med3_f32 v24, v24, s50, v190
	v_fma_f32 v24, v24, 4.0, 4.0
	v_mul_f32_e32 v22, v22, v25
	v_add_f32_e32 v25, 1.0, v27
	v_rcp_f32_e32 v25, v25
	v_mul_f32_e32 v24, v24, v22
	v_fmamk_f32 v22, v65, 0x39800000, v251
	v_med3_f32 v22, v22, s50, v190
	v_fma_f32 v22, v22, 4.0, 4.0
	v_mul_f32_e32 v25, v26, v25
	v_mul_f32_e32 v25, v22, v25
	v_fmamk_f32 v22, v50, 0x39800000, v244
	v_min_f32_e32 v22, 0x40e00000, v22
	v_mul_f32_e32 v27, 0xc01d265f, v22
	v_exp_f32_e32 v27, v27
	v_fmamk_f32 v28, v51, 0x39800000, v245
	v_min_f32_e32 v28, 0x40e00000, v28
	v_mul_f32_e32 v29, 0xc01d265f, v28
	v_add_f32_e32 v27, 1.0, v27
	v_rcp_f32_e32 v27, v27
	v_exp_f32_e32 v29, v29
	v_fmamk_f32 v26, v54, 0x39800000, v252
	v_med3_f32 v26, v26, s50, v190
	v_fma_f32 v26, v26, 4.0, 4.0
	v_mul_f32_e32 v22, v22, v27
	v_add_f32_e32 v27, 1.0, v29
	v_rcp_f32_e32 v27, v27
	v_mul_f32_e32 v26, v26, v22
	v_fmamk_f32 v22, v55, 0x39800000, v253
	v_med3_f32 v22, v22, s50, v190
	v_fma_f32 v22, v22, 4.0, 4.0
	v_mul_f32_e32 v27, v28, v27
	v_mul_f32_e32 v27, v22, v27
	v_fmamk_f32 v22, v52, 0x39800000, v246
	v_min_f32_e32 v22, 0x40e00000, v22
	v_mul_f32_e32 v29, 0xc01d265f, v22
	v_exp_f32_e32 v29, v29
	v_fmamk_f32 v30, v53, 0x39800000, v247
	v_min_f32_e32 v30, 0x40e00000, v30
	v_mul_f32_e32 v31, 0xc01d265f, v30
	v_add_f32_e32 v29, 1.0, v29
	v_rcp_f32_e32 v29, v29
	v_exp_f32_e32 v31, v31
	v_fmamk_f32 v28, v56, 0x39800000, v254
	v_med3_f32 v28, v28, s50, v190
	v_mul_f32_e32 v22, v22, v29
	v_add_f32_e32 v29, 1.0, v31
	v_rcp_f32_e32 v29, v29
	v_fma_f32 v28, v28, 4.0, 4.0
	v_mul_f32_e32 v28, v28, v22
	v_fmamk_f32 v22, v57, 0x39800000, v255
	v_mul_f32_e32 v29, v30, v29
	v_mov_b32_e32 v30, v24
	v_med3_f32 v22, v22, s50, v190
	v_mov_b32_e32 v31, v25
	v_cvt_pk_fp8_f32 v24, v21, v23
	v_mov_b32_e32 v21, v26
	v_mov_b32_e32 v23, v27
	v_fma_f32 v22, v22, 4.0, 4.0
	v_cvt_pk_fp8_f32 v25, v21, v23
	v_mul_f32_e32 v29, v22, v29
	v_fmamk_f32 v14, v42, 0x39800000, v240
	v_mov_b32_e32 v21, v28
	v_mov_b32_e32 v23, v29
	v_min_f32_e32 v14, 0x40e00000, v14
	v_cvt_pk_fp8_f32 v25, v21, v23 op_sel:[0,0,1]
	v_mul_f32_e32 v21, 0xc01d265f, v14
	v_add_u32_e32 v22, 0xa0, v20
	v_cvt_pk_fp8_f32 v24, v30, v31 op_sel:[0,0,1]
	v_ashrrev_i32_e32 v23, 31, v22
	v_exp_f32_e32 v21, v21
	v_lshlrev_b64 v[22:23], 11, v[22:23]
	v_lshl_add_u64 v[22:23], s[74:75], 0, v[22:23]
	v_fmamk_f32 v15, v43, 0x39800000, v241
	v_lshl_add_u64 v[22:23], v[22:23], 0, v[18:19]
	v_min_f32_e32 v15, 0x40e00000, v15
	global_store_dwordx2 v[22:23], v[24:25], off
	v_add_f32_e32 v21, 1.0, v21
	v_mul_f32_e32 v22, 0xc01d265f, v15
	v_rcp_f32_e32 v21, v21
	v_fmamk_f32 v10, v46, 0x39800000, v248
	v_exp_f32_e32 v22, v22
	v_med3_f32 v10, v10, s50, v190
	v_fma_f32 v10, v10, 4.0, 4.0
	v_mul_f32_e32 v14, v14, v21
	v_mul_f32_e32 v10, v10, v14
	v_add_f32_e32 v14, 1.0, v22
	v_rcp_f32_e32 v14, v14
	v_fmamk_f32 v11, v47, 0x39800000, v249
	v_med3_f32 v11, v11, s50, v190
	v_fma_f32 v11, v11, 4.0, 4.0
	v_mul_f32_e32 v14, v15, v14
	v_mul_f32_e32 v11, v11, v14
	v_fmamk_f32 v14, v44, 0x39800000, v242
	v_min_f32_e32 v14, 0x40e00000, v14
	v_mul_f32_e32 v15, 0xc01d265f, v14
	v_exp_f32_e32 v15, v15
	v_mov_b32_e32 v17, v243
	v_fmac_f32_e32 v17, 0x39800000, v45
	v_min_f32_e32 v16, 0x40e00000, v17
	v_mul_f32_e32 v17, 0xc01d265f, v16
	v_add_f32_e32 v15, 1.0, v15
	v_rcp_f32_e32 v15, v15
	v_fmamk_f32 v12, v48, 0x39800000, v250
	v_exp_f32_e32 v17, v17
	v_med3_f32 v12, v12, s50, v190
	v_fma_f32 v12, v12, 4.0, 4.0
	v_mul_f32_e32 v14, v14, v15
	v_mul_f32_e32 v12, v12, v14
	v_add_f32_e32 v14, 1.0, v17
	v_rcp_f32_e32 v14, v14
	v_mov_b32_e32 v13, v251
	v_fmac_f32_e32 v13, 0x39800000, v49
	v_med3_f32 v13, v13, s50, v190
	v_fma_f32 v13, v13, 4.0, 4.0
	v_fmamk_f32 v6, v38, 0x39800000, v244
	v_mul_f32_e32 v14, v16, v14
	v_min_f32_e32 v6, 0x40e00000, v6
	v_mul_f32_e32 v13, v13, v14
	v_mul_f32_e32 v14, 0xc01d265f, v6
	v_exp_f32_e32 v14, v14
	v_fmamk_f32 v7, v39, 0x39800000, v245
	v_min_f32_e32 v7, 0x40e00000, v7
	v_mul_f32_e32 v15, 0xc01d265f, v7
	v_add_f32_e32 v14, 1.0, v14
	v_rcp_f32_e32 v14, v14
	v_fmamk_f32 v2, v34, 0x39800000, v252
	v_exp_f32_e32 v15, v15
	v_med3_f32 v2, v2, s50, v190
	v_fma_f32 v2, v2, 4.0, 4.0
	v_mul_f32_e32 v6, v6, v14
	v_mul_f32_e32 v6, v2, v6
	v_fmamk_f32 v2, v35, 0x39800000, v253
	v_add_f32_e32 v3, 1.0, v15
	v_rcp_f32_e32 v3, v3
	v_med3_f32 v2, v2, s50, v190
	v_fma_f32 v2, v2, 4.0, 4.0
	v_mul_f32_e32 v3, v7, v3
	v_mul_f32_e32 v3, v2, v3
	v_fmamk_f32 v2, v40, 0x39800000, v246
	v_min_f32_e32 v2, 0x40e00000, v2
	v_mul_f32_e32 v7, 0xc01d265f, v2
	v_exp_f32_e32 v7, v7
	v_mov_b32_e32 v9, v247
	v_fmac_f32_e32 v9, 0x39800000, v41
	v_min_f32_e32 v8, 0x40e00000, v9
	v_mul_f32_e32 v9, 0xc01d265f, v8
	v_add_f32_e32 v7, 1.0, v7
	v_rcp_f32_e32 v7, v7
	v_fmamk_f32 v4, v36, 0x39800000, v254
	v_exp_f32_e32 v9, v9
	v_med3_f32 v4, v4, s50, v190
	v_fma_f32 v4, v4, 4.0, 4.0
	v_mul_f32_e32 v2, v2, v7
	v_mul_f32_e32 v7, v4, v2
	v_add_f32_e32 v2, 1.0, v9
	v_rcp_f32_e32 v2, v2
	v_mov_b32_e32 v5, v255
	v_fmac_f32_e32 v5, 0x39800000, v37
	v_med3_f32 v4, v5, s50, v190
	v_fma_f32 v4, v4, 4.0, 4.0
	v_mul_f32_e32 v2, v8, v2
	v_mul_f32_e32 v8, v4, v2
	v_mov_b32_e32 v5, v10
	v_mov_b32_e32 v9, v11
	v_cvt_pk_fp8_f32 v4, v5, v9
	v_cvt_pk_fp8_f32 v5, v6, v3
	v_add_u32_e32 v2, 0xb0, v20
	v_mov_b32_e32 v10, v12
	v_mov_b32_e32 v11, v13
	v_mov_b32_e32 v3, v7
	v_mov_b32_e32 v6, v8
	v_cvt_pk_fp8_f32 v4, v10, v11 op_sel:[0,0,1]
	v_cvt_pk_fp8_f32 v5, v3, v6 op_sel:[0,0,1]
	v_ashrrev_i32_e32 v3, 31, v2
	v_lshlrev_b64 v[2:3], 11, v[2:3]
	v_lshl_add_u64 v[2:3], s[74:75], 0, v[2:3]
	v_lshl_add_u64 v[2:3], v[2:3], 0, v[18:19]
	global_store_dwordx2 v[2:3], v[4:5], off
	s_cbranch_vccnz .LBB0_2527
	s_mov_b32 s6, s4
	s_mov_b32 s7, s4
	s_mov_b32 s5, s4
	v_mov_b64_e32 v[36:37], s[6:7]
	v_mov_b64_e32 v[160:161], s[6:7]
	v_mov_b64_e32 v[148:149], s[6:7]
	v_mov_b64_e32 v[140:141], s[6:7]
	v_mov_b64_e32 v[132:133], s[6:7]
	v_mov_b64_e32 v[124:125], s[6:7]
	v_mov_b64_e32 v[116:117], s[6:7]
	v_mov_b64_e32 v[108:109], s[6:7]
	v_mov_b64_e32 v[100:101], s[6:7]
	v_mov_b64_e32 v[156:157], s[6:7]
	v_mov_b64_e32 v[152:153], s[6:7]
	v_mov_b64_e32 v[144:145], s[6:7]
	v_mov_b64_e32 v[136:137], s[6:7]
	v_mov_b64_e32 v[128:129], s[6:7]
	v_mov_b64_e32 v[120:121], s[6:7]
	v_mov_b64_e32 v[112:113], s[6:7]
	v_mov_b64_e32 v[104:105], s[6:7]
	v_mov_b64_e32 v[92:93], s[6:7]
	v_mov_b64_e32 v[84:85], s[6:7]
	v_mov_b64_e32 v[76:77], s[6:7]
	v_mov_b64_e32 v[68:69], s[6:7]
	v_mov_b64_e32 v[60:61], s[6:7]
	v_mov_b64_e32 v[52:53], s[6:7]
	v_mov_b64_e32 v[44:45], s[6:7]
	v_mov_b64_e32 v[40:41], s[6:7]
	v_mov_b64_e32 v[96:97], s[6:7]
	v_mov_b64_e32 v[88:89], s[6:7]
	v_mov_b64_e32 v[80:81], s[6:7]
	v_mov_b64_e32 v[72:73], s[6:7]
	v_mov_b64_e32 v[64:65], s[6:7]
	v_mov_b64_e32 v[56:57], s[6:7]
	v_mov_b64_e32 v[48:49], s[6:7]
	v_mov_b64_e32 v[34:35], s[4:5]
	v_mov_b64_e32 v[158:159], s[4:5]
	v_mov_b64_e32 v[146:147], s[4:5]
	v_mov_b64_e32 v[138:139], s[4:5]
	v_mov_b64_e32 v[130:131], s[4:5]
	v_mov_b64_e32 v[122:123], s[4:5]
	v_mov_b64_e32 v[114:115], s[4:5]
	v_mov_b64_e32 v[106:107], s[4:5]
	v_mov_b64_e32 v[98:99], s[4:5]
	v_mov_b64_e32 v[154:155], s[4:5]
	v_mov_b64_e32 v[150:151], s[4:5]
	v_mov_b64_e32 v[142:143], s[4:5]
	v_mov_b64_e32 v[134:135], s[4:5]
	v_mov_b64_e32 v[126:127], s[4:5]
	v_mov_b64_e32 v[118:119], s[4:5]
	v_mov_b64_e32 v[110:111], s[4:5]
	v_mov_b64_e32 v[102:103], s[4:5]
	v_mov_b64_e32 v[90:91], s[4:5]
	v_mov_b64_e32 v[82:83], s[4:5]
	v_mov_b64_e32 v[74:75], s[4:5]
	v_mov_b64_e32 v[66:67], s[4:5]
	v_mov_b64_e32 v[58:59], s[4:5]
	v_mov_b64_e32 v[50:51], s[4:5]
	v_mov_b64_e32 v[42:43], s[4:5]
	v_mov_b64_e32 v[38:39], s[4:5]
	v_mov_b64_e32 v[94:95], s[4:5]
	v_mov_b64_e32 v[86:87], s[4:5]
	v_mov_b64_e32 v[78:79], s[4:5]
	v_mov_b64_e32 v[70:71], s[4:5]
	v_mov_b64_e32 v[62:63], s[4:5]
	v_mov_b64_e32 v[54:55], s[4:5]
	v_mov_b64_e32 v[46:47], s[4:5]
	s_andn2_b64 vcc, exec, s[8:9]
	s_cbranch_vccnz .LBB0_2526
	s_barrier
	s_branch .LBB0_2526
